# speedup vs baseline: 1.0105x; 1.0105x over previous
.Lpoll_w_g2:
	s_mov_b64 exec, s[100:101]
	s_barrier
	global_load_lds_dwordx4 v[6:7], off
	s_mov_b32 m0, s2
	v_mad_i64_i32 v[12:13], s[2:3], v174, s56, v[20:21]
	v_mad_i64_i32 v[10:11], s[2:3], v17, s56, v[12:13]
	v_add_u32_e32 v120, 0, v16
	global_load_lds_dwordx4 v[8:9], off
	v_readfirstlane_b32 s2, v120
	s_mov_b32 m0, s2
	v_mad_i64_i32 v[12:13], s[2:3], v18, s56, v[12:13]
	v_add_u32_e32 v122, 0x2000, v120
	v_mul_u32_u24_e32 v14, 0x24000, v14
	v_lshl_add_u64 v[10:11], v[10:11], 0, v[2:3]
	v_readfirstlane_b32 s2, v122
	v_lshlrev_b32_e32 v108, 1, v14
	global_load_lds_dwordx4 v[10:11], off
	s_mov_b32 m0, s2
	v_lshl_add_u64 v[14:15], s[42:43], 0, v[108:109]
	s_mov_b64 s[2:3], 0x24000
	v_lshl_add_u64 v[22:23], v[14:15], 0, s[2:3]
	v_readlane_b32 s4, v230, 7
	v_mad_i64_i32 v[24:25], s[2:3], v17, s56, v[22:23]
	s_nop 0
	v_add_u32_e32 v123, s4, v16
	v_lshl_add_u64 v[12:13], v[12:13], 0, v[4:5]
	v_readfirstlane_b32 s2, v123
	global_load_lds_dwordx4 v[12:13], off
	s_mov_b32 m0, s2
	v_mad_i64_i32 v[22:23], s[2:3], v18, s56, v[22:23]
	v_add_u32_e32 v19, s4, v19
	v_lshl_add_u64 v[24:25], v[24:25], 0, v[2:3]
	v_readfirstlane_b32 s2, v19
	v_or_b32_e32 v107, 0x80, v174
	global_load_lds_dwordx4 v[24:25], off
	v_lshl_add_u64 v[22:23], v[22:23], 0, v[4:5]
	s_mov_b32 m0, s2
	v_mad_i64_i32 v[20:21], s[2:3], v107, s56, v[20:21]
	global_load_lds_dwordx4 v[22:23], off
	v_mad_i64_i32 v[22:23], s[2:3], v17, s56, v[20:21]
	v_add_u32_e32 v125, 0x4000, v120
	v_add_u32_e32 v126, 0x6000, v120
	v_readfirstlane_b32 s2, v125
	s_mov_b32 m0, s2
	v_mad_i64_i32 v[20:21], s[2:3], v18, s56, v[20:21]
	v_lshl_add_u64 v[98:99], v[22:23], 0, v[2:3]
	v_readfirstlane_b32 s2, v126
	global_load_lds_dwordx4 v[98:99], off
	v_lshl_add_u64 v[100:101], v[20:21], 0, v[4:5]
	s_mov_b32 m0, s2
	v_and_b32_e32 v19, 0xffffff00, v175
	global_load_lds_dwordx4 v[100:101], off
	s_movk_i32 s2, 0x100
	v_cmp_eq_u32_e32 vcc, s2, v19
	s_and_saveexec_b64 s[2:3], vcc
	s_cbranch_execz .LBB1_51
	s_barrier
	s_setprio 1

.LBB1_52:
	ds_read_b128 v[138:141], v135
	ds_read_b128 v[142:145], v135 offset:1024
	ds_read_b128 v[146:149], v135 offset:2048
	ds_read_b128 v[150:153], v135 offset:3072
	ds_read_b128 v[154:157], v135 offset:4096
	ds_read_b128 v[158:161], v135 offset:5120
	s_add_u32 m0, s12, 0xc000
	ds_read_b128 v[162:165], v121
	ds_read_b128 v[182:185], v121 offset:1024
	ds_read_b128 v[186:189], v108
	ds_read_b128 v[190:193], v108 offset:1024
	global_load_lds_dwordx4 v236, s[8:9]
	s_add_u32 m0, s12, 0xe000
	s_nop 0
	global_load_lds_dwordx4 v237, s[8:9]
	s_waitcnt lgkmcnt(4)
	s_barrier
	s_waitcnt lgkmcnt(0)
	s_waitcnt lgkmcnt(0)
	v_mfma_f32_16x16x32_f16 v[94:97], v[162:165], v[138:141], v[94:97]
	v_mfma_f32_16x16x32_f16 v[90:93], v[162:165], v[146:149], v[90:93]
	v_mfma_f32_16x16x32_f16 v[86:89], v[162:165], v[154:157], v[86:89]
	v_mfma_f32_16x16x32_f16 v[82:85], v[186:189], v[138:141], v[82:85]
	v_mfma_f32_16x16x32_f16 v[78:81], v[186:189], v[146:149], v[78:81]
	v_mfma_f32_16x16x32_f16 v[66:69], v[186:189], v[154:157], v[66:69]
	v_mfma_f32_16x16x32_f16 v[94:97], v[182:185], v[142:145], v[94:97]
	v_mfma_f32_16x16x32_f16 v[90:93], v[182:185], v[150:153], v[90:93]
	v_mfma_f32_16x16x32_f16 v[86:89], v[182:185], v[158:161], v[86:89]
	v_mfma_f32_16x16x32_f16 v[82:85], v[190:193], v[142:145], v[82:85]
	v_mfma_f32_16x16x32_f16 v[78:81], v[190:193], v[150:153], v[78:81]
	v_mfma_f32_16x16x32_f16 v[66:69], v[190:193], v[158:161], v[66:69]
	s_barrier
	s_add_u32 m0, s12, 0x10000
	ds_read_b128 v[194:197], v134
	ds_read_b128 v[198:201], v134 offset:1024
	ds_read_b128 v[202:205], v134 offset:2048
	ds_read_b128 v[206:209], v134 offset:3072
	ds_read_b128 v[210:213], v134 offset:4096
	ds_read_b128 v[214:217], v134 offset:5120
	global_load_lds_dwordx4 v240, s[10:11]
	s_add_u32 m0, s12, 0x12000
	s_nop 0
	global_load_lds_dwordx4 v241, s[10:11]
	s_barrier
	s_waitcnt lgkmcnt(0)
	s_waitcnt lgkmcnt(0)
	v_mfma_f32_16x16x32_f16 v[22:25], v[162:165], v[194:197], v[22:25]
	v_mfma_f32_16x16x32_f16 v[18:21], v[162:165], v[202:205], v[18:21]
	v_mfma_f32_16x16x32_f16 v[14:17], v[162:165], v[210:213], v[14:17]
	v_mfma_f32_16x16x32_f16 v[10:13], v[186:189], v[194:197], v[10:13]
	v_mfma_f32_16x16x32_f16 v[6:9], v[186:189], v[202:205], v[6:9]
	v_mfma_f32_16x16x32_f16 v[2:5], v[186:189], v[210:213], v[2:5]
	v_mfma_f32_16x16x32_f16 v[22:25], v[182:185], v[198:201], v[22:25]
	v_mfma_f32_16x16x32_f16 v[18:21], v[182:185], v[206:209], v[18:21]
	v_mfma_f32_16x16x32_f16 v[14:17], v[182:185], v[214:217], v[14:17]
	v_mfma_f32_16x16x32_f16 v[10:13], v[190:193], v[198:201], v[10:13]
	v_mfma_f32_16x16x32_f16 v[6:9], v[190:193], v[206:209], v[6:9]
	v_mfma_f32_16x16x32_f16 v[2:5], v[190:193], v[214:217], v[2:5]
	s_add_u32 m0, s12, 0x0
	s_barrier
	ds_read_b128 v[162:165], v121 offset:16384
	ds_read_b128 v[182:185], v121 offset:17408
	ds_read_b128 v[186:189], v108 offset:16384
	ds_read_b128 v[190:193], v108 offset:17408
	global_load_lds_dwordx4 v232, s[8:9]
	s_add_u32 m0, s12, 0x2000
	s_nop 0
	global_load_lds_dwordx4 v233, s[8:9]
	s_barrier
	s_waitcnt lgkmcnt(0)
	s_waitcnt lgkmcnt(0)
	v_mfma_f32_16x16x32_f16 v[26:29], v[162:165], v[138:141], v[26:29]
	v_mfma_f32_16x16x32_f16 v[30:33], v[162:165], v[146:149], v[30:33]
	v_mfma_f32_16x16x32_f16 v[34:37], v[162:165], v[154:157], v[34:37]
	v_mfma_f32_16x16x32_f16 v[38:41], v[186:189], v[138:141], v[38:41]
	v_mfma_f32_16x16x32_f16 v[46:49], v[186:189], v[146:149], v[46:49]
	v_mfma_f32_16x16x32_f16 v[54:57], v[186:189], v[154:157], v[54:57]
	v_mfma_f32_16x16x32_f16 v[26:29], v[182:185], v[142:145], v[26:29]
	v_mfma_f32_16x16x32_f16 v[30:33], v[182:185], v[150:153], v[30:33]
	v_mfma_f32_16x16x32_f16 v[34:37], v[182:185], v[158:161], v[34:37]
	v_mfma_f32_16x16x32_f16 v[38:41], v[190:193], v[142:145], v[38:41]
	v_mfma_f32_16x16x32_f16 v[46:49], v[190:193], v[150:153], v[46:49]
	v_mfma_f32_16x16x32_f16 v[54:57], v[190:193], v[158:161], v[54:57]
	s_barrier
	s_add_u32 m0, s12, 0x14000
	s_nop 0
	global_load_lds_dwordx4 v244, s[10:11]
	s_add_u32 m0, s12, 0x16000
	s_nop 0
	global_load_lds_dwordx4 v245, s[10:11]
	s_waitcnt vmcnt(6)
	s_barrier
	v_mfma_f32_16x16x32_f16 v[42:45], v[162:165], v[194:197], v[42:45]
	v_mfma_f32_16x16x32_f16 v[50:53], v[162:165], v[202:205], v[50:53]
	v_mfma_f32_16x16x32_f16 v[58:61], v[162:165], v[210:213], v[58:61]
	v_mfma_f32_16x16x32_f16 v[62:65], v[186:189], v[194:197], v[62:65]
	v_mfma_f32_16x16x32_f16 v[70:73], v[186:189], v[202:205], v[70:73]
	v_mfma_f32_16x16x32_f16 v[74:77], v[186:189], v[210:213], v[74:77]
	v_mfma_f32_16x16x32_f16 v[42:45], v[182:185], v[198:201], v[42:45]
	v_mfma_f32_16x16x32_f16 v[50:53], v[182:185], v[206:209], v[50:53]
	v_mfma_f32_16x16x32_f16 v[58:61], v[182:185], v[214:217], v[58:61]
	v_mfma_f32_16x16x32_f16 v[62:65], v[190:193], v[198:201], v[62:65]
	v_mfma_f32_16x16x32_f16 v[70:73], v[190:193], v[206:209], v[70:73]
	v_mfma_f32_16x16x32_f16 v[74:77], v[190:193], v[214:217], v[74:77]
	s_barrier
	ds_read_b128 v[138:141], v127
	ds_read_b128 v[142:145], v127 offset:1024
	ds_read_b128 v[146:149], v127 offset:2048
	ds_read_b128 v[150:153], v127 offset:3072
	ds_read_b128 v[154:157], v127 offset:4096
	ds_read_b128 v[158:161], v127 offset:5120
	s_add_u32 m0, s12, 0x4000
	ds_read_b128 v[162:165], v121 offset:32768
	ds_read_b128 v[182:185], v121 offset:33792
	ds_read_b128 v[186:189], v108 offset:32768
	ds_read_b128 v[190:193], v108 offset:33792
	global_load_lds_dwordx4 v238, s[8:9]
	s_add_u32 m0, s12, 0x6000
	s_nop 0
	global_load_lds_dwordx4 v239, s[8:9]
	s_waitcnt lgkmcnt(4)
	s_barrier
	s_waitcnt lgkmcnt(0)
	s_waitcnt lgkmcnt(0)
	v_mfma_f32_16x16x32_f16 v[94:97], v[162:165], v[138:141], v[94:97]
	v_mfma_f32_16x16x32_f16 v[90:93], v[162:165], v[146:149], v[90:93]
	v_mfma_f32_16x16x32_f16 v[86:89], v[162:165], v[154:157], v[86:89]
	v_mfma_f32_16x16x32_f16 v[82:85], v[186:189], v[138:141], v[82:85]
	v_mfma_f32_16x16x32_f16 v[78:81], v[186:189], v[146:149], v[78:81]
	v_mfma_f32_16x16x32_f16 v[66:69], v[186:189], v[154:157], v[66:69]
	v_mfma_f32_16x16x32_f16 v[94:97], v[182:185], v[142:145], v[94:97]
	v_mfma_f32_16x16x32_f16 v[90:93], v[182:185], v[150:153], v[90:93]
	v_mfma_f32_16x16x32_f16 v[86:89], v[182:185], v[158:161], v[86:89]
	v_mfma_f32_16x16x32_f16 v[82:85], v[190:193], v[142:145], v[82:85]
	v_mfma_f32_16x16x32_f16 v[78:81], v[190:193], v[150:153], v[78:81]
	v_mfma_f32_16x16x32_f16 v[66:69], v[190:193], v[158:161], v[66:69]
	s_barrier
	s_add_u32 m0, s12, 0x18000
	ds_read_b128 v[194:197], v124
	ds_read_b128 v[198:201], v124 offset:1024
	ds_read_b128 v[202:205], v124 offset:2048
	ds_read_b128 v[206:209], v124 offset:3072
	ds_read_b128 v[210:213], v124 offset:4096
	ds_read_b128 v[214:217], v124 offset:5120
	global_load_lds_dwordx4 v242, s[10:11]
	s_add_u32 m0, s12, 0x1a000
	s_nop 0
	global_load_lds_dwordx4 v243, s[10:11]
	s_barrier
	s_waitcnt lgkmcnt(0)
	s_waitcnt lgkmcnt(0)
	v_mfma_f32_16x16x32_f16 v[22:25], v[162:165], v[194:197], v[22:25]
	v_mfma_f32_16x16x32_f16 v[18:21], v[162:165], v[202:205], v[18:21]
	v_mfma_f32_16x16x32_f16 v[14:17], v[162:165], v[210:213], v[14:17]
	v_mfma_f32_16x16x32_f16 v[10:13], v[186:189], v[194:197], v[10:13]
	v_mfma_f32_16x16x32_f16 v[6:9], v[186:189], v[202:205], v[6:9]
	v_mfma_f32_16x16x32_f16 v[2:5], v[186:189], v[210:213], v[2:5]
	v_mfma_f32_16x16x32_f16 v[22:25], v[182:185], v[198:201], v[22:25]
	v_mfma_f32_16x16x32_f16 v[18:21], v[182:185], v[206:209], v[18:21]
	v_mfma_f32_16x16x32_f16 v[14:17], v[182:185], v[214:217], v[14:17]
	v_mfma_f32_16x16x32_f16 v[10:13], v[190:193], v[198:201], v[10:13]
	v_mfma_f32_16x16x32_f16 v[6:9], v[190:193], v[206:209], v[6:9]
	v_mfma_f32_16x16x32_f16 v[2:5], v[190:193], v[214:217], v[2:5]
	s_add_u32 m0, s12, 0x8000
	s_barrier
	ds_read_b128 v[162:165], v121 offset:49152
	ds_read_b128 v[182:185], v121 offset:50176
	ds_read_b128 v[186:189], v108 offset:49152
	ds_read_b128 v[190:193], v108 offset:50176
	global_load_lds_dwordx4 v234, s[8:9]
	s_add_u32 m0, s12, 0xa000
	s_nop 0
	global_load_lds_dwordx4 v235, s[8:9]
	s_barrier
	s_waitcnt lgkmcnt(0)
	s_waitcnt lgkmcnt(0)
	v_mfma_f32_16x16x32_f16 v[26:29], v[162:165], v[138:141], v[26:29]
	v_mfma_f32_16x16x32_f16 v[30:33], v[162:165], v[146:149], v[30:33]
	v_mfma_f32_16x16x32_f16 v[34:37], v[162:165], v[154:157], v[34:37]
	v_mfma_f32_16x16x32_f16 v[38:41], v[186:189], v[138:141], v[38:41]
	v_mfma_f32_16x16x32_f16 v[46:49], v[186:189], v[146:149], v[46:49]
	v_mfma_f32_16x16x32_f16 v[54:57], v[186:189], v[154:157], v[54:57]
	v_mfma_f32_16x16x32_f16 v[26:29], v[182:185], v[142:145], v[26:29]
	v_mfma_f32_16x16x32_f16 v[30:33], v[182:185], v[150:153], v[30:33]
	v_mfma_f32_16x16x32_f16 v[34:37], v[182:185], v[158:161], v[34:37]
	v_mfma_f32_16x16x32_f16 v[38:41], v[190:193], v[142:145], v[38:41]
	v_mfma_f32_16x16x32_f16 v[46:49], v[190:193], v[150:153], v[46:49]
	v_mfma_f32_16x16x32_f16 v[54:57], v[190:193], v[158:161], v[54:57]
	s_barrier
	s_add_u32 m0, s12, 0x1c000
	s_nop 0
	global_load_lds_dwordx4 v246, s[10:11]
	s_add_u32 m0, s12, 0x1e000
	s_nop 0
	global_load_lds_dwordx4 v247, s[10:11]
	s_waitcnt vmcnt(6)
	s_barrier
	v_mfma_f32_16x16x32_f16 v[42:45], v[162:165], v[194:197], v[42:45]
	v_mfma_f32_16x16x32_f16 v[50:53], v[162:165], v[202:205], v[50:53]
	v_mfma_f32_16x16x32_f16 v[58:61], v[162:165], v[210:213], v[58:61]
	v_mfma_f32_16x16x32_f16 v[62:65], v[186:189], v[194:197], v[62:65]
	v_mfma_f32_16x16x32_f16 v[70:73], v[186:189], v[202:205], v[70:73]
	v_mfma_f32_16x16x32_f16 v[74:77], v[186:189], v[210:213], v[74:77]
	v_mfma_f32_16x16x32_f16 v[42:45], v[182:185], v[198:201], v[42:45]
	v_mfma_f32_16x16x32_f16 v[50:53], v[182:185], v[206:209], v[50:53]
	v_mfma_f32_16x16x32_f16 v[58:61], v[182:185], v[214:217], v[58:61]
	v_mfma_f32_16x16x32_f16 v[62:65], v[190:193], v[198:201], v[62:65]
	v_mfma_f32_16x16x32_f16 v[70:73], v[190:193], v[206:209], v[70:73]
	v_mfma_f32_16x16x32_f16 v[74:77], v[190:193], v[214:217], v[74:77]
	s_add_i32 s4, s4, 2
	s_add_u32 s2, s2, 0x100
	s_addc_u32 s3, s3, 0
	s_add_u32 s8, s8, 0x100
	s_addc_u32 s9, s9, 0
	s_add_u32 s10, s10, 0x100
	s_addc_u32 s11, s11, 0
	s_cmp_lt_u32 s4, 8
	s_barrier
	s_cbranch_scc1 .LBB1_52
	s_mov_b64 s[4:5], 0x580
	v_readfirstlane_b32 s2, v136
	v_lshl_add_u64 v[98:99], v[98:99], 0, s[4:5]
	s_mov_b32 m0, s2
	v_readfirstlane_b32 s2, v137
	ds_read_b128 v[102:105], v135
	ds_read_b128 v[110:113], v135 offset:1024
	ds_read_b128 v[114:117], v135 offset:2048
	ds_read_b128 v[128:131], v135 offset:3072
	ds_read_b128 v[138:141], v135 offset:4096
	ds_read_b128 v[142:145], v135 offset:5120
	ds_read_b128 v[146:149], v121
	ds_read_b128 v[150:153], v121 offset:1024
	ds_read_b128 v[154:157], v108
	ds_read_b128 v[158:161], v108 offset:1024
	global_load_lds_dwordx4 v[98:99], off
	v_lshl_add_u64 v[98:99], v[100:101], 0, s[4:5]
	s_mov_b32 m0, s2
	s_nop 0
	global_load_lds_dwordx4 v[98:99], off
	s_barrier
	s_waitcnt lgkmcnt(0)
	s_setprio 1
	s_waitcnt lgkmcnt(0)
	v_mfma_f32_16x16x32_f16 v[94:97], v[146:149], v[102:105], v[94:97]
	v_mfma_f32_16x16x32_f16 v[90:93], v[146:149], v[114:117], v[90:93]
	v_mfma_f32_16x16x32_f16 v[86:89], v[146:149], v[138:141], v[86:89]
	v_mfma_f32_16x16x32_f16 v[82:85], v[154:157], v[102:105], v[82:85]
	v_mfma_f32_16x16x32_f16 v[78:81], v[154:157], v[114:117], v[78:81]
	v_mfma_f32_16x16x32_f16 v[66:69], v[154:157], v[138:141], v[66:69]
	v_mfma_f32_16x16x32_f16 v[94:97], v[150:153], v[110:113], v[94:97]
	v_mfma_f32_16x16x32_f16 v[90:93], v[150:153], v[128:131], v[90:93]
	v_mfma_f32_16x16x32_f16 v[86:89], v[150:153], v[142:145], v[86:89]
	v_mfma_f32_16x16x32_f16 v[82:85], v[158:161], v[110:113], v[82:85]
	v_mfma_f32_16x16x32_f16 v[98:101], v[158:161], v[128:131], v[78:81]
	v_mfma_f32_16x16x32_f16 v[66:69], v[158:161], v[142:145], v[66:69]
	s_setprio 0
	s_barrier
	ds_read_b128 v[78:81], v134
	ds_read_b128 v[162:165], v134 offset:1024
	ds_read_b128 v[182:185], v134 offset:2048
	ds_read_b128 v[186:189], v134 offset:3072
	ds_read_b128 v[190:193], v134 offset:4096
	ds_read_b128 v[132:135], v134 offset:5120
	s_barrier
	s_waitcnt lgkmcnt(0)
	s_setprio 1
	s_waitcnt lgkmcnt(0)
	v_mfma_f32_16x16x32_f16 v[22:25], v[146:149], v[78:81], v[22:25]
	v_mfma_f32_16x16x32_f16 v[18:21], v[146:149], v[182:185], v[18:21]
	v_mfma_f32_16x16x32_f16 v[14:17], v[146:149], v[190:193], v[14:17]
	v_mfma_f32_16x16x32_f16 v[10:13], v[154:157], v[78:81], v[10:13]
	v_mfma_f32_16x16x32_f16 v[6:9], v[154:157], v[182:185], v[6:9]
	v_mfma_f32_16x16x32_f16 v[2:5], v[154:157], v[190:193], v[2:5]
	v_mfma_f32_16x16x32_f16 v[22:25], v[150:153], v[162:165], v[22:25]
	v_mfma_f32_16x16x32_f16 v[18:21], v[150:153], v[186:189], v[18:21]
	v_mfma_f32_16x16x32_f16 v[14:17], v[150:153], v[132:135], v[14:17]
	v_mfma_f32_16x16x32_f16 v[10:13], v[158:161], v[162:165], v[10:13]
	v_mfma_f32_16x16x32_f16 v[6:9], v[158:161], v[186:189], v[6:9]
	v_mfma_f32_16x16x32_f16 v[2:5], v[158:161], v[132:135], v[2:5]
	s_setprio 0
	s_barrier
	ds_read_b128 v[146:149], v121 offset:16384
	ds_read_b128 v[150:153], v121 offset:17408
	ds_read_b128 v[154:157], v108 offset:16384
	ds_read_b128 v[158:161], v108 offset:17408
	s_waitcnt vmcnt(4)
	s_barrier
	s_waitcnt lgkmcnt(0)
	s_setprio 1
	s_waitcnt lgkmcnt(0)
	v_mfma_f32_16x16x32_f16 v[26:29], v[146:149], v[102:105], v[26:29]
	v_mfma_f32_16x16x32_f16 v[30:33], v[146:149], v[114:117], v[30:33]
	v_mfma_f32_16x16x32_f16 v[34:37], v[146:149], v[138:141], v[34:37]
	v_mfma_f32_16x16x32_f16 v[38:41], v[154:157], v[102:105], v[38:41]
	v_mfma_f32_16x16x32_f16 v[46:49], v[154:157], v[114:117], v[46:49]
	v_mfma_f32_16x16x32_f16 v[26:29], v[150:153], v[110:113], v[26:29]
	v_mfma_f32_16x16x32_f16 v[30:33], v[150:153], v[128:131], v[30:33]
	v_mfma_f32_16x16x32_f16 v[34:37], v[150:153], v[142:145], v[34:37]
	v_mfma_f32_16x16x32_f16 v[38:41], v[158:161], v[110:113], v[38:41]
	v_mfma_f32_16x16x32_f16 v[46:49], v[158:161], v[128:131], v[46:49]
	v_mfma_f32_16x16x32_f16 v[54:57], v[154:157], v[138:141], v[54:57]
	v_mfma_f32_16x16x32_f16 v[54:57], v[158:161], v[142:145], v[54:57]
	s_setprio 0
	s_setprio 1
	v_mfma_f32_16x16x32_f16 v[58:61], v[146:149], v[190:193], v[58:61]
	v_mfma_f32_16x16x32_f16 v[110:113], v[150:153], v[132:135], v[58:61]
	v_mfma_f32_16x16x32_f16 v[58:61], v[154:157], v[78:81], v[62:65]
	v_mfma_f32_16x16x32_f16 v[42:45], v[146:149], v[78:81], v[42:45]
	v_mfma_f32_16x16x32_f16 v[114:117], v[158:161], v[162:165], v[58:61]
	v_mfma_f32_16x16x32_f16 v[58:61], v[154:157], v[182:185], v[70:73]
	v_mfma_f32_16x16x32_f16 v[42:45], v[150:153], v[162:165], v[42:45]
	v_mfma_f32_16x16x32_f16 v[50:53], v[146:149], v[182:185], v[50:53]
	v_mfma_f32_16x16x32_f16 v[128:131], v[158:161], v[186:189], v[58:61]
	v_mfma_f32_16x16x32_f16 v[58:61], v[154:157], v[190:193], v[74:77]
	v_mfma_f32_16x16x32_f16 v[50:53], v[150:153], v[186:189], v[50:53]
	v_mfma_f32_16x16x32_f16 v[132:135], v[158:161], v[132:135], v[58:61]
	s_setprio 0
	s_barrier
	ds_read_b128 v[136:139], v127
	ds_read_b128 v[140:143], v127 offset:1024
	ds_read_b128 v[144:147], v127 offset:2048
	ds_read_b128 v[148:151], v127 offset:3072
	ds_read_b128 v[152:155], v127 offset:4096
	ds_read_b128 v[156:159], v127 offset:5120
	ds_read_b128 v[74:77], v121 offset:32768
	ds_read_b128 v[160:163], v121 offset:33792
	ds_read_b128 v[164:167], v108 offset:32768
	ds_read_b128 v[182:185], v108 offset:33792
	s_waitcnt vmcnt(2)
	s_barrier
	s_waitcnt lgkmcnt(0)
	s_setprio 1
	s_waitcnt lgkmcnt(0)
	v_mfma_f32_16x16x32_f16 v[62:65], v[74:77], v[144:147], v[90:93]
	v_mfma_f32_16x16x32_f16 v[70:73], v[164:167], v[136:139], v[82:85]
	v_mfma_f32_16x16x32_f16 v[58:61], v[74:77], v[136:139], v[94:97]
	v_mfma_f32_16x16x32_f16 v[78:81], v[160:163], v[148:151], v[62:65]
	v_mfma_f32_16x16x32_f16 v[62:65], v[74:77], v[152:155], v[86:89]
	v_mfma_f32_16x16x32_f16 v[102:105], v[182:185], v[140:143], v[70:73]
	v_mfma_f32_16x16x32_f16 v[70:73], v[164:167], v[144:147], v[98:101]
	v_mfma_f32_16x16x32_f16 v[66:69], v[164:167], v[152:155], v[66:69]
	v_mfma_f32_16x16x32_f16 v[58:61], v[160:163], v[140:143], v[58:61]
	v_mfma_f32_16x16x32_f16 v[62:65], v[160:163], v[156:159], v[62:65]
	v_mfma_f32_16x16x32_f16 v[86:89], v[182:185], v[148:151], v[70:73]
	v_mfma_f32_16x16x32_f16 v[70:73], v[182:185], v[156:159], v[66:69]
	s_setprio 0
	s_barrier
	ds_read_b128 v[186:189], v124
	ds_read_b128 v[190:193], v124 offset:1024
	ds_read_b128 v[194:197], v124 offset:2048
	ds_read_b128 v[198:201], v124 offset:3072
	ds_read_b128 v[202:205], v124 offset:4096
	ds_read_b128 v[122:125], v124 offset:5120
	s_waitcnt vmcnt(0)
	s_barrier
	s_waitcnt lgkmcnt(0)
	s_setprio 1
	s_waitcnt lgkmcnt(0)
	v_mfma_f32_16x16x32_f16 v[22:25], v[74:77], v[186:189], v[22:25]
	v_mfma_f32_16x16x32_f16 v[18:21], v[74:77], v[194:197], v[18:21]
	v_mfma_f32_16x16x32_f16 v[14:17], v[74:77], v[202:205], v[14:17]
	v_mfma_f32_16x16x32_f16 v[10:13], v[164:167], v[186:189], v[10:13]
	v_mfma_f32_16x16x32_f16 v[6:9], v[164:167], v[194:197], v[6:9]
	v_mfma_f32_16x16x32_f16 v[2:5], v[164:167], v[202:205], v[2:5]
	v_mfma_f32_16x16x32_f16 v[94:97], v[160:163], v[190:193], v[22:25]
	v_mfma_f32_16x16x32_f16 v[82:85], v[160:163], v[198:201], v[18:21]
	v_mfma_f32_16x16x32_f16 v[66:69], v[160:163], v[122:125], v[14:17]
	v_mfma_f32_16x16x32_f16 v[98:101], v[182:185], v[190:193], v[10:13]
	v_mfma_f32_16x16x32_f16 v[90:93], v[182:185], v[198:201], v[6:9]
	v_mfma_f32_16x16x32_f16 v[74:77], v[182:185], v[122:125], v[2:5]
	s_setprio 0
	s_barrier
	ds_read_b128 v[10:13], v121 offset:49152
	ds_read_b128 v[160:163], v121 offset:50176
	ds_read_b128 v[164:167], v108 offset:49152
	ds_read_b128 v[182:185], v108 offset:50176
	s_barrier
	s_waitcnt lgkmcnt(0)
	s_setprio 1
	s_waitcnt lgkmcnt(0)
	v_mfma_f32_16x16x32_f16 v[2:5], v[10:13], v[136:139], v[26:29]
	v_mfma_f32_16x16x32_f16 v[18:21], v[164:167], v[136:139], v[38:41]
	v_mfma_f32_16x16x32_f16 v[14:17], v[160:163], v[140:143], v[2:5]
	v_mfma_f32_16x16x32_f16 v[2:5], v[10:13], v[144:147], v[30:33]
	v_mfma_f32_16x16x32_f16 v[38:41], v[182:185], v[140:143], v[18:21]
	v_mfma_f32_16x16x32_f16 v[18:21], v[164:167], v[144:147], v[46:49]
	v_mfma_f32_16x16x32_f16 v[6:9], v[160:163], v[148:151], v[2:5]
	v_mfma_f32_16x16x32_f16 v[2:5], v[10:13], v[152:155], v[34:37]
	v_mfma_f32_16x16x32_f16 v[26:29], v[182:185], v[148:151], v[18:21]
	v_mfma_f32_16x16x32_f16 v[18:21], v[164:167], v[152:155], v[54:57]
	v_mfma_f32_16x16x32_f16 v[2:5], v[160:163], v[156:159], v[2:5]
	v_mfma_f32_16x16x32_f16 v[18:21], v[182:185], v[156:159], v[18:21]
	s_setprio 0
	s_setprio 1
	v_mfma_f32_16x16x32_f16 v[34:37], v[164:167], v[186:189], v[114:117]
	v_mfma_f32_16x16x32_f16 v[22:25], v[10:13], v[186:189], v[42:45]
	v_mfma_f32_16x16x32_f16 v[46:49], v[182:185], v[190:193], v[34:37]
	v_mfma_f32_16x16x32_f16 v[34:37], v[164:167], v[194:197], v[128:131]
	v_mfma_f32_16x16x32_f16 v[30:33], v[160:163], v[190:193], v[22:25]
	v_mfma_f32_16x16x32_f16 v[22:25], v[10:13], v[194:197], v[50:53]
	v_mfma_f32_16x16x32_f16 v[10:13], v[10:13], v[202:205], v[110:113]
	v_mfma_f32_16x16x32_f16 v[42:45], v[182:185], v[198:201], v[34:37]
	v_mfma_f32_16x16x32_f16 v[34:37], v[164:167], v[202:205], v[132:135]
	v_mfma_f32_16x16x32_f16 v[22:25], v[160:163], v[198:201], v[22:25]
	v_mfma_f32_16x16x32_f16 v[10:13], v[160:163], v[122:125], v[10:13]
	v_mfma_f32_16x16x32_f16 v[34:37], v[182:185], v[122:125], v[34:37]
	s_setprio 0
	s_movk_i32 s2, 0x100
	v_cmp_gt_u32_e32 vcc, s2, v175
	s_barrier
	s_and_saveexec_b64 s[2:3], vcc
	s_cbranch_execz .LBB1_55
	s_barrier

.Lpoll_done_g1:
	global_load_lds_dwordx4 v[6:7], off
	s_mov_b32 m0, s0
	v_mad_i64_i32 v[12:13], s[0:1], v120, s56, v[20:21]
	v_mad_i64_i32 v[10:11], s[0:1], v17, s56, v[12:13]
	v_add_u32_e32 v129, 0, v16
	global_load_lds_dwordx4 v[8:9], off
	v_readfirstlane_b32 s0, v129
	s_mov_b32 m0, s0
	v_mad_i64_i32 v[12:13], s[0:1], v18, s56, v[12:13]
	v_add_u32_e32 v131, 0x2000, v129
	v_mul_u32_u24_e32 v14, 0x24000, v14
	v_lshl_add_u64 v[10:11], v[10:11], 0, v[2:3]
	v_readfirstlane_b32 s0, v131
	v_lshlrev_b32_e32 v108, 1, v14
	global_load_lds_dwordx4 v[10:11], off
	s_mov_b32 m0, s0
	v_lshl_add_u64 v[14:15], s[40:41], 0, v[108:109]
	s_mov_b64 s[0:1], 0x24000
	v_lshl_add_u64 v[22:23], v[14:15], 0, s[0:1]
	v_readlane_b32 s2, v230, 7
	v_mad_i64_i32 v[24:25], s[0:1], v17, s56, v[22:23]
	s_nop 0
	v_add_u32_e32 v132, s2, v16
	v_lshl_add_u64 v[12:13], v[12:13], 0, v[4:5]
	v_readfirstlane_b32 s0, v132
	global_load_lds_dwordx4 v[12:13], off
	s_mov_b32 m0, s0
	v_mad_i64_i32 v[22:23], s[0:1], v18, s56, v[22:23]
	v_add_u32_e32 v19, s2, v19
	v_lshl_add_u64 v[24:25], v[24:25], 0, v[2:3]
	v_readfirstlane_b32 s0, v19
	v_or_b32_e32 v19, 0x80, v120
	global_load_lds_dwordx4 v[24:25], off
	v_lshl_add_u64 v[22:23], v[22:23], 0, v[4:5]
	s_mov_b32 m0, s0
	v_mad_i64_i32 v[20:21], s[0:1], v19, s56, v[20:21]
	global_load_lds_dwordx4 v[22:23], off
	v_mad_i64_i32 v[22:23], s[0:1], v17, s56, v[20:21]
	v_add_u32_e32 v134, 0x4000, v129
	v_add_u32_e32 v135, 0x6000, v129
	v_readfirstlane_b32 s0, v134
	s_mov_b32 m0, s0
	v_mad_i64_i32 v[20:21], s[0:1], v18, s56, v[20:21]
	v_lshl_add_u64 v[100:101], v[22:23], 0, v[2:3]
	v_readfirstlane_b32 s0, v135
	global_load_lds_dwordx4 v[100:101], off
	v_lshl_add_u64 v[102:103], v[20:21], 0, v[4:5]
	s_mov_b32 m0, s0
	v_and_b32_e32 v19, 0xffffff00, v107
	global_load_lds_dwordx4 v[102:103], off
	s_movk_i32 s0, 0x100
	v_cmp_eq_u32_e64 s[0:1], s0, v19
	s_and_saveexec_b64 s[2:3], s[0:1]
	s_cbranch_execz .LBB1_65
	s_barrier
	s_setprio 1

.LBB1_66:
	ds_read_b128 v[148:151], v144
	ds_read_b128 v[152:155], v144 offset:1024
	ds_read_b128 v[156:159], v144 offset:2048
	ds_read_b128 v[160:163], v144 offset:3072
	ds_read_b128 v[164:167], v144 offset:4096
	ds_read_b128 v[174:177], v144 offset:5120
	s_add_u32 m0, s12, 0xc000
	ds_read_b128 v[178:181], v130
	ds_read_b128 v[182:185], v130 offset:1024
	ds_read_b128 v[186:189], v108
	ds_read_b128 v[190:193], v108 offset:1024
	global_load_lds_dwordx4 v236, s[8:9]
	s_add_u32 m0, s12, 0xe000
	s_nop 0
	global_load_lds_dwordx4 v237, s[8:9]
	s_waitcnt lgkmcnt(4)
	s_barrier
	s_waitcnt lgkmcnt(0)
	s_waitcnt lgkmcnt(0)
	v_mfma_f32_16x16x32_f16 v[94:97], v[178:181], v[148:151], v[94:97]
	v_mfma_f32_16x16x32_f16 v[90:93], v[178:181], v[156:159], v[90:93]
	v_mfma_f32_16x16x32_f16 v[86:89], v[178:181], v[164:167], v[86:89]
	v_mfma_f32_16x16x32_f16 v[74:77], v[186:189], v[148:151], v[74:77]
	v_mfma_f32_16x16x32_f16 v[46:49], v[186:189], v[156:159], v[46:49]
	v_mfma_f32_16x16x32_f16 v[18:21], v[186:189], v[164:167], v[18:21]
	v_mfma_f32_16x16x32_f16 v[94:97], v[182:185], v[152:155], v[94:97]
	v_mfma_f32_16x16x32_f16 v[90:93], v[182:185], v[160:163], v[90:93]
	v_mfma_f32_16x16x32_f16 v[86:89], v[182:185], v[174:177], v[86:89]
	v_mfma_f32_16x16x32_f16 v[74:77], v[190:193], v[152:155], v[74:77]
	v_mfma_f32_16x16x32_f16 v[46:49], v[190:193], v[160:163], v[46:49]
	v_mfma_f32_16x16x32_f16 v[18:21], v[190:193], v[174:177], v[18:21]
	s_barrier
	s_add_u32 m0, s12, 0x10000
	ds_read_b128 v[194:197], v143
	ds_read_b128 v[198:201], v143 offset:1024
	ds_read_b128 v[202:205], v143 offset:2048
	ds_read_b128 v[206:209], v143 offset:3072
	ds_read_b128 v[210:213], v143 offset:4096
	ds_read_b128 v[214:217], v143 offset:5120
	global_load_lds_dwordx4 v240, s[10:11]
	s_add_u32 m0, s12, 0x12000
	s_nop 0
	global_load_lds_dwordx4 v241, s[10:11]
	s_barrier
	s_waitcnt lgkmcnt(0)
	s_waitcnt lgkmcnt(0)
	v_mfma_f32_16x16x32_f16 v[10:13], v[178:181], v[194:197], v[10:13]
	v_mfma_f32_16x16x32_f16 v[6:9], v[178:181], v[202:205], v[6:9]
	v_mfma_f32_16x16x32_f16 v[2:5], v[178:181], v[210:213], v[2:5]
	v_mfma_f32_16x16x32_f16 v[26:29], v[186:189], v[194:197], v[26:29]
	v_mfma_f32_16x16x32_f16 v[34:37], v[186:189], v[202:205], v[34:37]
	v_mfma_f32_16x16x32_f16 v[50:53], v[186:189], v[210:213], v[50:53]
	v_mfma_f32_16x16x32_f16 v[10:13], v[182:185], v[198:201], v[10:13]
	v_mfma_f32_16x16x32_f16 v[6:9], v[182:185], v[206:209], v[6:9]
	v_mfma_f32_16x16x32_f16 v[2:5], v[182:185], v[214:217], v[2:5]
	v_mfma_f32_16x16x32_f16 v[26:29], v[190:193], v[198:201], v[26:29]
	v_mfma_f32_16x16x32_f16 v[34:37], v[190:193], v[206:209], v[34:37]
	v_mfma_f32_16x16x32_f16 v[50:53], v[190:193], v[214:217], v[50:53]
	s_add_u32 m0, s12, 0x0
	s_barrier
	ds_read_b128 v[178:181], v130 offset:16384
	ds_read_b128 v[182:185], v130 offset:17408
	ds_read_b128 v[186:189], v108 offset:16384
	ds_read_b128 v[190:193], v108 offset:17408
	global_load_lds_dwordx4 v232, s[8:9]
	s_add_u32 m0, s12, 0x2000
	s_nop 0
	global_load_lds_dwordx4 v233, s[8:9]
	s_barrier
	s_waitcnt lgkmcnt(0)
	s_waitcnt lgkmcnt(0)
	v_mfma_f32_16x16x32_f16 v[14:17], v[178:181], v[148:151], v[14:17]
	v_mfma_f32_16x16x32_f16 v[22:25], v[178:181], v[156:159], v[22:25]
	v_mfma_f32_16x16x32_f16 v[30:33], v[178:181], v[164:167], v[30:33]
	v_mfma_f32_16x16x32_f16 v[38:41], v[186:189], v[148:151], v[38:41]
	v_mfma_f32_16x16x32_f16 v[54:57], v[186:189], v[156:159], v[54:57]
	v_mfma_f32_16x16x32_f16 v[62:65], v[186:189], v[164:167], v[62:65]
	v_mfma_f32_16x16x32_f16 v[14:17], v[182:185], v[152:155], v[14:17]
	v_mfma_f32_16x16x32_f16 v[22:25], v[182:185], v[160:163], v[22:25]
	v_mfma_f32_16x16x32_f16 v[30:33], v[182:185], v[174:177], v[30:33]
	v_mfma_f32_16x16x32_f16 v[38:41], v[190:193], v[152:155], v[38:41]
	v_mfma_f32_16x16x32_f16 v[54:57], v[190:193], v[160:163], v[54:57]
	v_mfma_f32_16x16x32_f16 v[62:65], v[190:193], v[174:177], v[62:65]
	s_barrier
	s_add_u32 m0, s12, 0x14000
	s_nop 0
	global_load_lds_dwordx4 v244, s[10:11]
	s_add_u32 m0, s12, 0x16000
	s_nop 0
	global_load_lds_dwordx4 v245, s[10:11]
	s_waitcnt vmcnt(6)
	s_barrier
	v_mfma_f32_16x16x32_f16 v[42:45], v[178:181], v[194:197], v[42:45]
	v_mfma_f32_16x16x32_f16 v[58:61], v[178:181], v[202:205], v[58:61]
	v_mfma_f32_16x16x32_f16 v[66:69], v[178:181], v[210:213], v[66:69]
	v_mfma_f32_16x16x32_f16 v[70:73], v[186:189], v[194:197], v[70:73]
	v_mfma_f32_16x16x32_f16 v[78:81], v[186:189], v[202:205], v[78:81]
	v_mfma_f32_16x16x32_f16 v[82:85], v[186:189], v[210:213], v[82:85]
	v_mfma_f32_16x16x32_f16 v[42:45], v[182:185], v[198:201], v[42:45]
	v_mfma_f32_16x16x32_f16 v[58:61], v[182:185], v[206:209], v[58:61]
	v_mfma_f32_16x16x32_f16 v[66:69], v[182:185], v[214:217], v[66:69]
	v_mfma_f32_16x16x32_f16 v[70:73], v[190:193], v[198:201], v[70:73]
	v_mfma_f32_16x16x32_f16 v[78:81], v[190:193], v[206:209], v[78:81]
	v_mfma_f32_16x16x32_f16 v[82:85], v[190:193], v[214:217], v[82:85]
	s_barrier
	ds_read_b128 v[148:151], v136
	ds_read_b128 v[152:155], v136 offset:1024
	ds_read_b128 v[156:159], v136 offset:2048
	ds_read_b128 v[160:163], v136 offset:3072
	ds_read_b128 v[164:167], v136 offset:4096
	ds_read_b128 v[174:177], v136 offset:5120
	s_add_u32 m0, s12, 0x4000
	ds_read_b128 v[178:181], v130 offset:32768
	ds_read_b128 v[182:185], v130 offset:33792
	ds_read_b128 v[186:189], v108 offset:32768
	ds_read_b128 v[190:193], v108 offset:33792
	global_load_lds_dwordx4 v238, s[8:9]
	s_add_u32 m0, s12, 0x6000
	s_nop 0
	global_load_lds_dwordx4 v239, s[8:9]
	s_waitcnt lgkmcnt(4)
	s_barrier
	s_waitcnt lgkmcnt(0)
	s_waitcnt lgkmcnt(0)
	v_mfma_f32_16x16x32_f16 v[94:97], v[178:181], v[148:151], v[94:97]
	v_mfma_f32_16x16x32_f16 v[90:93], v[178:181], v[156:159], v[90:93]
	v_mfma_f32_16x16x32_f16 v[86:89], v[178:181], v[164:167], v[86:89]
	v_mfma_f32_16x16x32_f16 v[74:77], v[186:189], v[148:151], v[74:77]
	v_mfma_f32_16x16x32_f16 v[46:49], v[186:189], v[156:159], v[46:49]
	v_mfma_f32_16x16x32_f16 v[18:21], v[186:189], v[164:167], v[18:21]
	v_mfma_f32_16x16x32_f16 v[94:97], v[182:185], v[152:155], v[94:97]
	v_mfma_f32_16x16x32_f16 v[90:93], v[182:185], v[160:163], v[90:93]
	v_mfma_f32_16x16x32_f16 v[86:89], v[182:185], v[174:177], v[86:89]
	v_mfma_f32_16x16x32_f16 v[74:77], v[190:193], v[152:155], v[74:77]
	v_mfma_f32_16x16x32_f16 v[46:49], v[190:193], v[160:163], v[46:49]
	v_mfma_f32_16x16x32_f16 v[18:21], v[190:193], v[174:177], v[18:21]
	s_barrier
	s_add_u32 m0, s12, 0x18000
	ds_read_b128 v[194:197], v133
	ds_read_b128 v[198:201], v133 offset:1024
	ds_read_b128 v[202:205], v133 offset:2048
	ds_read_b128 v[206:209], v133 offset:3072
	ds_read_b128 v[210:213], v133 offset:4096
	ds_read_b128 v[214:217], v133 offset:5120
	global_load_lds_dwordx4 v242, s[10:11]
	s_add_u32 m0, s12, 0x1a000
	s_nop 0
	global_load_lds_dwordx4 v243, s[10:11]
	s_barrier
	s_waitcnt lgkmcnt(0)
	s_waitcnt lgkmcnt(0)
	v_mfma_f32_16x16x32_f16 v[10:13], v[178:181], v[194:197], v[10:13]
	v_mfma_f32_16x16x32_f16 v[6:9], v[178:181], v[202:205], v[6:9]
	v_mfma_f32_16x16x32_f16 v[2:5], v[178:181], v[210:213], v[2:5]
	v_mfma_f32_16x16x32_f16 v[26:29], v[186:189], v[194:197], v[26:29]
	v_mfma_f32_16x16x32_f16 v[34:37], v[186:189], v[202:205], v[34:37]
	v_mfma_f32_16x16x32_f16 v[50:53], v[186:189], v[210:213], v[50:53]
	v_mfma_f32_16x16x32_f16 v[10:13], v[182:185], v[198:201], v[10:13]
	v_mfma_f32_16x16x32_f16 v[6:9], v[182:185], v[206:209], v[6:9]
	v_mfma_f32_16x16x32_f16 v[2:5], v[182:185], v[214:217], v[2:5]
	v_mfma_f32_16x16x32_f16 v[26:29], v[190:193], v[198:201], v[26:29]
	v_mfma_f32_16x16x32_f16 v[34:37], v[190:193], v[206:209], v[34:37]
	v_mfma_f32_16x16x32_f16 v[50:53], v[190:193], v[214:217], v[50:53]
	s_add_u32 m0, s12, 0x8000
	s_barrier
	ds_read_b128 v[178:181], v130 offset:49152
	ds_read_b128 v[182:185], v130 offset:50176
	ds_read_b128 v[186:189], v108 offset:49152
	ds_read_b128 v[190:193], v108 offset:50176
	global_load_lds_dwordx4 v234, s[8:9]
	s_add_u32 m0, s12, 0xa000
	s_nop 0
	global_load_lds_dwordx4 v235, s[8:9]
	s_barrier
	s_waitcnt lgkmcnt(0)
	s_waitcnt lgkmcnt(0)
	v_mfma_f32_16x16x32_f16 v[14:17], v[178:181], v[148:151], v[14:17]
	v_mfma_f32_16x16x32_f16 v[22:25], v[178:181], v[156:159], v[22:25]
	v_mfma_f32_16x16x32_f16 v[30:33], v[178:181], v[164:167], v[30:33]
	v_mfma_f32_16x16x32_f16 v[38:41], v[186:189], v[148:151], v[38:41]
	v_mfma_f32_16x16x32_f16 v[54:57], v[186:189], v[156:159], v[54:57]
	v_mfma_f32_16x16x32_f16 v[62:65], v[186:189], v[164:167], v[62:65]
	v_mfma_f32_16x16x32_f16 v[14:17], v[182:185], v[152:155], v[14:17]
	v_mfma_f32_16x16x32_f16 v[22:25], v[182:185], v[160:163], v[22:25]
	v_mfma_f32_16x16x32_f16 v[30:33], v[182:185], v[174:177], v[30:33]
	v_mfma_f32_16x16x32_f16 v[38:41], v[190:193], v[152:155], v[38:41]
	v_mfma_f32_16x16x32_f16 v[54:57], v[190:193], v[160:163], v[54:57]
	v_mfma_f32_16x16x32_f16 v[62:65], v[190:193], v[174:177], v[62:65]
	s_barrier
	s_add_u32 m0, s12, 0x1c000
	s_nop 0
	global_load_lds_dwordx4 v246, s[10:11]
	s_add_u32 m0, s12, 0x1e000
	s_nop 0
	global_load_lds_dwordx4 v247, s[10:11]
	s_waitcnt vmcnt(6)
	s_barrier
	v_mfma_f32_16x16x32_f16 v[42:45], v[178:181], v[194:197], v[42:45]
	v_mfma_f32_16x16x32_f16 v[58:61], v[178:181], v[202:205], v[58:61]
	v_mfma_f32_16x16x32_f16 v[66:69], v[178:181], v[210:213], v[66:69]
	v_mfma_f32_16x16x32_f16 v[70:73], v[186:189], v[194:197], v[70:73]
	v_mfma_f32_16x16x32_f16 v[78:81], v[186:189], v[202:205], v[78:81]
	v_mfma_f32_16x16x32_f16 v[82:85], v[186:189], v[210:213], v[82:85]
	v_mfma_f32_16x16x32_f16 v[42:45], v[182:185], v[198:201], v[42:45]
	v_mfma_f32_16x16x32_f16 v[58:61], v[182:185], v[206:209], v[58:61]
	v_mfma_f32_16x16x32_f16 v[66:69], v[182:185], v[214:217], v[66:69]
	v_mfma_f32_16x16x32_f16 v[70:73], v[190:193], v[198:201], v[70:73]
	v_mfma_f32_16x16x32_f16 v[78:81], v[190:193], v[206:209], v[78:81]
	v_mfma_f32_16x16x32_f16 v[82:85], v[190:193], v[214:217], v[82:85]
	s_add_i32 s2, s2, 2
	s_add_u32 s0, s0, 0x100
	s_addc_u32 s1, s1, 0
	s_add_u32 s8, s8, 0x100
	s_addc_u32 s9, s9, 0
	s_add_u32 s10, s10, 0x100
	s_addc_u32 s11, s11, 0
	s_cmp_lt_u32 s2, 8
	s_barrier
	s_cbranch_scc1 .LBB1_66
	v_readlane_b32 s10, v230, 2
	v_readlane_b32 s11, v230, 3
	v_or_b32_e32 v238, v126, v125
	v_add_u32_e32 v238, v238, v121
	v_lshlrev_b32_e32 v232, 1, v238
	v_and_b32_e32 v232, -4, v232
	v_add_u32_e32 v233, 16, v238
	v_lshlrev_b32_e32 v233, 1, v233
	v_and_b32_e32 v233, -4, v233
	v_add_u32_e32 v234, 32, v238
	v_lshlrev_b32_e32 v234, 1, v234
	v_and_b32_e32 v234, -4, v234
	v_add_u32_e32 v235, 0x60, v238
	v_lshlrev_b32_e32 v235, 1, v235
	v_and_b32_e32 v235, -4, v235
	v_add_u32_e32 v236, 0x70, v238
	v_lshlrev_b32_e32 v236, 1, v236
	v_and_b32_e32 v236, -4, v236
	v_add_u32_e32 v237, 0x80, v238
	v_lshlrev_b32_e32 v237, 1, v237
	v_and_b32_e32 v237, -4, v237
	global_load_dword v232, v232, s[48:49]
	global_load_dword v233, v233, s[48:49]
	global_load_dword v234, v234, s[48:49]
	global_load_dword v235, v235, s[48:49]
	global_load_dword v236, v236, s[48:49]
	global_load_dword v237, v237, s[48:49]
	s_mov_b32 s32, 0x2aaaaaab
	v_mul_hi_u32 v239, v107, s32
	v_lshrrev_b32_e32 v239, 4, v239
	v_mul_u32_u24_e32 v239, 0x60, v239
	v_sub_u32_e32 v239, v107, v239
	v_lshrrev_b32_e32 v240, 1, v121
	v_add_u32_e32 v239, v239, v240
	v_lshlrev_b32_e32 v239, 3, v239
	global_load_dwordx2 v[240:241], v239, s[10:11]
	global_load_dwordx2 v[242:243], v239, s[10:11] offset:3072
	s_mov_b64 s[2:3], 0x580
	v_readfirstlane_b32 s0, v145
	v_lshl_add_u64 v[100:101], v[100:101], 0, s[2:3]
	s_mov_b32 m0, s0
	v_readfirstlane_b32 s0, v146
	ds_read_b128 v[110:113], v144
	ds_read_b128 v[114:117], v144 offset:1024
	ds_read_b128 v[138:141], v144 offset:2048
	ds_read_b128 v[148:151], v144 offset:3072
	ds_read_b128 v[152:155], v144 offset:4096
	ds_read_b128 v[156:159], v144 offset:5120
	ds_read_b128 v[160:163], v130
	ds_read_b128 v[164:167], v130 offset:1024
	ds_read_b128 v[174:177], v108
	ds_read_b128 v[178:181], v108 offset:1024
	global_load_lds_dwordx4 v[100:101], off
	v_lshl_add_u64 v[100:101], v[102:103], 0, s[2:3]
	s_mov_b32 m0, s0
	s_nop 0
	global_load_lds_dwordx4 v[100:101], off
	s_barrier
	s_waitcnt lgkmcnt(0)
	s_setprio 1
	s_waitcnt lgkmcnt(0)
	v_mfma_f32_16x16x32_f16 v[94:97], v[160:163], v[110:113], v[94:97]
	v_mfma_f32_16x16x32_f16 v[90:93], v[160:163], v[138:141], v[90:93]
	v_mfma_f32_16x16x32_f16 v[86:89], v[160:163], v[152:155], v[86:89]
	v_mfma_f32_16x16x32_f16 v[74:77], v[174:177], v[110:113], v[74:77]
	v_mfma_f32_16x16x32_f16 v[18:21], v[174:177], v[152:155], v[18:21]
	v_mfma_f32_16x16x32_f16 v[94:97], v[164:167], v[114:117], v[94:97]
	v_mfma_f32_16x16x32_f16 v[90:93], v[164:167], v[148:151], v[90:93]
	v_mfma_f32_16x16x32_f16 v[86:89], v[164:167], v[156:159], v[86:89]
	v_mfma_f32_16x16x32_f16 v[74:77], v[178:181], v[114:117], v[74:77]
	v_mfma_f32_16x16x32_f16 v[46:49], v[174:177], v[138:141], v[46:49]
	v_mfma_f32_16x16x32_f16 v[18:21], v[178:181], v[156:159], v[18:21]
	v_mfma_f32_16x16x32_f16 v[100:103], v[178:181], v[148:151], v[46:49]
	s_setprio 0
	s_barrier
	s_nop 3
	ds_read_b128 v[46:49], v143
	ds_read_b128 v[144:147], v143 offset:1024
	ds_read_b128 v[182:185], v143 offset:2048
	ds_read_b128 v[186:189], v143 offset:3072
	ds_read_b128 v[190:193], v143 offset:4096
	ds_read_b128 v[194:197], v143 offset:5120
	s_barrier
	s_waitcnt lgkmcnt(0)
	s_setprio 1
	s_waitcnt lgkmcnt(0)
	v_mfma_f32_16x16x32_f16 v[34:37], v[174:177], v[182:185], v[34:37]
	v_mfma_f32_16x16x32_f16 v[10:13], v[160:163], v[46:49], v[10:13]
	v_mfma_f32_16x16x32_f16 v[6:9], v[160:163], v[182:185], v[6:9]
	v_mfma_f32_16x16x32_f16 v[2:5], v[160:163], v[190:193], v[2:5]
	v_mfma_f32_16x16x32_f16 v[26:29], v[174:177], v[46:49], v[26:29]
	v_mfma_f32_16x16x32_f16 v[160:163], v[178:181], v[186:189], v[34:37]
	v_mfma_f32_16x16x32_f16 v[34:37], v[174:177], v[190:193], v[50:53]
	v_mfma_f32_16x16x32_f16 v[10:13], v[164:167], v[144:147], v[10:13]
	v_mfma_f32_16x16x32_f16 v[6:9], v[164:167], v[186:189], v[6:9]
	v_mfma_f32_16x16x32_f16 v[2:5], v[164:167], v[194:197], v[2:5]
	v_mfma_f32_16x16x32_f16 v[26:29], v[178:181], v[144:147], v[26:29]
	v_mfma_f32_16x16x32_f16 v[50:53], v[178:181], v[194:197], v[34:37]
	s_setprio 0
	s_barrier
	s_nop 0
	ds_read_b128 v[34:37], v130 offset:16384
	ds_read_b128 v[164:167], v130 offset:17408
	ds_read_b128 v[174:177], v108 offset:16384
	ds_read_b128 v[178:181], v108 offset:17408
	s_waitcnt vmcnt(12)
	s_barrier
	s_waitcnt lgkmcnt(0)
	s_setprio 1
	s_waitcnt lgkmcnt(0)
	v_mfma_f32_16x16x32_f16 v[22:25], v[34:37], v[138:141], v[22:25]
	v_mfma_f32_16x16x32_f16 v[198:201], v[164:167], v[148:151], v[22:25]
	v_mfma_f32_16x16x32_f16 v[22:25], v[34:37], v[152:155], v[30:33]
	v_mfma_f32_16x16x32_f16 v[30:33], v[164:167], v[156:159], v[22:25]
	v_mfma_f32_16x16x32_f16 v[22:25], v[174:177], v[110:113], v[38:41]
	v_mfma_f32_16x16x32_f16 v[14:17], v[34:37], v[110:113], v[14:17]
	v_mfma_f32_16x16x32_f16 v[110:113], v[178:181], v[114:117], v[22:25]
	v_mfma_f32_16x16x32_f16 v[22:25], v[174:177], v[138:141], v[54:57]
	v_mfma_f32_16x16x32_f16 v[14:17], v[164:167], v[114:117], v[14:17]
	v_mfma_f32_16x16x32_f16 v[54:57], v[178:181], v[148:151], v[22:25]
	v_mfma_f32_16x16x32_f16 v[22:25], v[174:177], v[152:155], v[62:65]
	v_mfma_f32_16x16x32_f16 v[114:117], v[178:181], v[156:159], v[22:25]
	s_setprio 0
	s_setprio 1
	v_mfma_f32_16x16x32_f16 v[22:25], v[34:37], v[46:49], v[42:45]
	v_mfma_f32_16x16x32_f16 v[138:141], v[164:167], v[144:147], v[22:25]
	v_mfma_f32_16x16x32_f16 v[22:25], v[34:37], v[182:185], v[58:61]
	v_mfma_f32_16x16x32_f16 v[148:151], v[164:167], v[186:189], v[22:25]
	v_mfma_f32_16x16x32_f16 v[22:25], v[34:37], v[190:193], v[66:69]
	v_mfma_f32_16x16x32_f16 v[152:155], v[164:167], v[194:197], v[22:25]
	v_mfma_f32_16x16x32_f16 v[22:25], v[174:177], v[46:49], v[70:73]
	v_mfma_f32_16x16x32_f16 v[142:145], v[178:181], v[144:147], v[22:25]
	v_mfma_f32_16x16x32_f16 v[22:25], v[174:177], v[182:185], v[78:81]
	v_mfma_f32_16x16x32_f16 v[156:159], v[178:181], v[186:189], v[22:25]
	v_mfma_f32_16x16x32_f16 v[22:25], v[174:177], v[190:193], v[82:85]
	v_mfma_f32_16x16x32_f16 v[164:167], v[178:181], v[194:197], v[22:25]
	s_setprio 0
	s_barrier
	ds_read_b128 v[58:61], v136
	ds_read_b128 v[174:177], v136 offset:1024
	ds_read_b128 v[178:181], v136 offset:2048
	ds_read_b128 v[182:185], v136 offset:3072
	ds_read_b128 v[186:189], v136 offset:4096
	ds_read_b128 v[134:137], v136 offset:5120
	ds_read_b128 v[34:37], v130 offset:32768
	ds_read_b128 v[62:65], v130 offset:33792
	ds_read_b128 v[78:81], v108 offset:32768
	ds_read_b128 v[190:193], v108 offset:33792
	s_waitcnt vmcnt(2)
	s_barrier
	s_waitcnt lgkmcnt(0)
	s_setprio 1
	s_waitcnt lgkmcnt(0)
	v_mfma_f32_16x16x32_f16 v[22:25], v[34:37], v[58:61], v[94:97]
	v_mfma_f32_16x16x32_f16 v[82:85], v[62:65], v[174:177], v[22:25]
	v_mfma_f32_16x16x32_f16 v[22:25], v[34:37], v[178:181], v[90:93]
	v_mfma_f32_16x16x32_f16 v[70:73], v[62:65], v[182:185], v[22:25]
	v_mfma_f32_16x16x32_f16 v[22:25], v[34:37], v[186:189], v[86:89]
	v_mfma_f32_16x16x32_f16 v[46:49], v[62:65], v[134:137], v[22:25]
	v_mfma_f32_16x16x32_f16 v[22:25], v[78:81], v[58:61], v[74:77]
	v_mfma_f32_16x16x32_f16 v[86:89], v[190:193], v[174:177], v[22:25]
	v_mfma_f32_16x16x32_f16 v[22:25], v[78:81], v[178:181], v[100:103]
	v_mfma_f32_16x16x32_f16 v[18:21], v[78:81], v[186:189], v[18:21]
	v_mfma_f32_16x16x32_f16 v[66:69], v[190:193], v[182:185], v[22:25]
	v_mfma_f32_16x16x32_f16 v[42:45], v[190:193], v[134:137], v[18:21]
	s_setprio 0
	s_barrier
	ds_read_b128 v[100:103], v133
	ds_read_b128 v[194:197], v133 offset:1024
	ds_read_b128 v[202:205], v133 offset:2048
	ds_read_b128 v[206:209], v133 offset:3072
	ds_read_b128 v[210:213], v133 offset:4096
	ds_read_b128 v[214:217], v133 offset:5120
	s_waitcnt vmcnt(0)
	s_barrier
	s_waitcnt lgkmcnt(0)
	s_setprio 1
	s_waitcnt lgkmcnt(0)
	v_mfma_f32_16x16x32_f16 v[6:9], v[34:37], v[202:205], v[6:9]
	v_mfma_f32_16x16x32_f16 v[2:5], v[34:37], v[210:213], v[2:5]
	v_mfma_f32_16x16x32_f16 v[22:25], v[62:65], v[206:209], v[6:9]
	v_mfma_f32_16x16x32_f16 v[6:9], v[62:65], v[214:217], v[2:5]
	v_mfma_f32_16x16x32_f16 v[2:5], v[78:81], v[100:103], v[26:29]
	v_mfma_f32_16x16x32_f16 v[10:13], v[34:37], v[100:103], v[10:13]
	v_mfma_f32_16x16x32_f16 v[34:37], v[190:193], v[194:197], v[2:5]
	v_mfma_f32_16x16x32_f16 v[2:5], v[78:81], v[202:205], v[160:163]
	v_mfma_f32_16x16x32_f16 v[18:21], v[190:193], v[206:209], v[2:5]
	v_mfma_f32_16x16x32_f16 v[2:5], v[78:81], v[210:213], v[50:53]
	v_mfma_f32_16x16x32_f16 v[38:41], v[62:65], v[194:197], v[10:13]
	v_mfma_f32_16x16x32_f16 v[2:5], v[190:193], v[214:217], v[2:5]
	s_setprio 0
	s_barrier
	ds_read_b128 v[10:13], v130 offset:49152
	ds_read_b128 v[26:29], v130 offset:50176
	ds_read_b128 v[128:131], v108 offset:49152
	ds_read_b128 v[160:163], v108 offset:50176
	s_barrier
	s_waitcnt lgkmcnt(0)
	s_setprio 1
	s_waitcnt lgkmcnt(0)
	v_mfma_f32_16x16x32_f16 v[14:17], v[10:13], v[58:61], v[14:17]
	v_mfma_f32_16x16x32_f16 v[90:93], v[26:29], v[174:177], v[14:17]
	v_mfma_f32_16x16x32_f16 v[14:17], v[10:13], v[178:181], v[198:201]
	v_mfma_f32_16x16x32_f16 v[78:81], v[26:29], v[182:185], v[14:17]
	v_mfma_f32_16x16x32_f16 v[14:17], v[10:13], v[186:189], v[30:33]
	v_mfma_f32_16x16x32_f16 v[62:65], v[26:29], v[134:137], v[14:17]
	v_mfma_f32_16x16x32_f16 v[14:17], v[128:131], v[58:61], v[110:113]
	v_mfma_f32_16x16x32_f16 v[94:97], v[160:163], v[174:177], v[14:17]
	v_mfma_f32_16x16x32_f16 v[14:17], v[128:131], v[178:181], v[54:57]
	v_mfma_f32_16x16x32_f16 v[74:77], v[160:163], v[182:185], v[14:17]
	v_mfma_f32_16x16x32_f16 v[14:17], v[128:131], v[186:189], v[114:117]
	v_mfma_f32_16x16x32_f16 v[58:61], v[160:163], v[134:137], v[14:17]
	s_setprio 0
	s_setprio 1
	v_mfma_f32_16x16x32_f16 v[14:17], v[10:13], v[100:103], v[138:141]
	v_mfma_f32_16x16x32_f16 v[54:57], v[26:29], v[194:197], v[14:17]
	v_mfma_f32_16x16x32_f16 v[14:17], v[10:13], v[202:205], v[148:151]
	v_mfma_f32_16x16x32_f16 v[10:13], v[10:13], v[210:213], v[152:155]
	v_mfma_f32_16x16x32_f16 v[30:33], v[26:29], v[206:209], v[14:17]
	v_mfma_f32_16x16x32_f16 v[14:17], v[26:29], v[214:217], v[10:13]
	v_mfma_f32_16x16x32_f16 v[10:13], v[128:131], v[100:103], v[142:145]
	v_mfma_f32_16x16x32_f16 v[50:53], v[160:163], v[194:197], v[10:13]
	v_mfma_f32_16x16x32_f16 v[10:13], v[128:131], v[202:205], v[156:159]
	v_mfma_f32_16x16x32_f16 v[26:29], v[160:163], v[206:209], v[10:13]
	v_mfma_f32_16x16x32_f16 v[10:13], v[128:131], v[210:213], v[164:167]
	v_mfma_f32_16x16x32_f16 v[10:13], v[160:163], v[214:217], v[10:13]
	s_setprio 0
	s_movk_i32 s0, 0x100
	v_cmp_gt_u32_e64 s[0:1], s0, v107
	s_barrier
	s_and_saveexec_b64 s[2:3], s[0:1]
	s_cbranch_execz .LBB1_69
	s_barrier
